# P12: down-weight conversion slots staggered by half-XCD (slot = (c&7 + 4*(c>>7)) & 7): 16 instead of 32 workgroups of one XCD convert together
# speedup vs baseline: 1.1564x; 1.0384x over previous
; __device__ __forceinline__ int lane_id_now() { unsigned z = 0u; asm volatile("" : "+v"(z)); return (int)__builtin_amdgcn_mbcnt_hi(~0u, __builtin_amdgcn_mbcnt_lo(~0u, z)); }
; #define PG8_STAGE(bufoff, gbase, voff) do { _Pragma("unroll") for (int _i = 0; _i < 2; ++_i) \
;         __builtin_amdgcn_global_load_lds((const unsigned*)((const char*)(gbase) + (voff)[_i]), (PG8_LAS unsigned*)(lds + (bufoff) + ldsw + _i * 8192), 16, 0, 0); } while (0)
; #define PG8_WAIT_V(n) asm volatile("s_waitcnt vmcnt(" #n ")" ::: "memory")
; #define PG8_BAR __builtin_amdgcn_s_barrier()
; template <class Epi, class Sched, bool ALIGN_EPI = false, bool SP2 = false>
; __device__ __forceinline__ void gemm_phase(PG8_LAS unsigned char* lds, const Geo geo, const Sched& S, const Epi& E, const int wave_) {
;     ...
;     PG8_STAGE(PG8_SB(1, 0), cB + kstep, voffB); PG8_STAGE(PG8_SA(1, 0), cA + kstep, c0); PG8_STAGE(PG8_SB(1, 1), cB + hstepB + kstep, voffB);
;     PG8_WAIT_V(6); PG8_BAR;
;     __device__ __forceinline__ void convert_share() const {
;         const int lane = lane_id_now(), gw = c * NWAVES + wave, NGW = G * NWAVES;
;         constexpr int NIT = E * (FF / 128) * (D / 32);
;         TSTREAM(NIT, dec_dn, TI8L_NT, TI8S_NT);
;     }
;     __device__ __forceinline__ void done(const Unit& u) const { if (u.pm == (c & 7)) convert_share(); }
.LBB0_1517:
	s_add_u32 s63, s78, 0x57dc8000
	s_addc_u32 s64, s79, 0
	s_add_u32 s14, s78, 0x6d7c8000
	s_addc_u32 s15, s79, 0
	s_add_u32 s93, s78, 0x23dc8000
	s_addc_u32 s9, s79, 0
	s_lshl_b32 s13, s0, 6
	s_lshl_b32 s26, s0, 13
	s_lshl_b32 s0, s1, 5
	s_and_b32 s20, s0, 0x60
	s_lshl_b32 s4, s20, 7
	s_add_i32 s70, s31, 0x18000
	s_mov_b64 s[16:17], 0x80
	s_add_i32 s72, s31, 0x1a000
	v_lshl_add_u64 v[2:3], v[2:3], 0, s[16:17]
	s_mov_b32 m0, s70
	s_add_u32 s18, s78, 0x67dc8080
	s_waitcnt vmcnt(2)
	s_barrier
	global_load_lds_dwordx4 v[2:3], off
	v_lshl_add_u64 v[0:1], v[0:1], 0, s[16:17]
	s_mov_b32 m0, s72
	s_addc_u32 s19, s79, 0
	s_add_i32 s74, s31, 0x8000
	s_add_i32 s82, s31, 0xa000
	global_load_lds_dwordx4 v[0:1], off
	v_lshl_add_u64 v[0:1], s[18:19], 0, v[64:65]
	s_mov_b32 m0, s74
	s_add_u32 s0, s6, 0x400080
	global_load_lds_dwordx4 v[0:1], off
	v_lshl_add_u64 v[0:1], s[18:19], 0, v[200:201]
	s_mov_b32 m0, s82
	s_addc_u32 s1, s7, 0
	s_add_i32 s95, s31, 0x1c000
	global_load_lds_dwordx4 v[0:1], off
	v_lshl_add_u64 v[0:1], s[0:1], 0, v[196:197]
	s_mov_b32 m0, s95
	s_add_i32 s97, s31, 0x1e000
	global_load_lds_dwordx4 v[0:1], off
	v_lshl_add_u64 v[0:1], s[0:1], 0, v[198:199]
	s_mov_b32 m0, s97
	s_add_i32 s4, s4, 0
	global_load_lds_dwordx4 v[0:1], off
	s_cmpk_lt_u32 s2, 0x100
	s_cselect_b64 s[24:25], -1, 0
	s_and_b32 s0, s92, 7
	s_bfe_u32 s3, s92, 0x10007
	s_lshl_b32 s3, s3, 2
	s_add_i32 s0, s0, s3
	s_and_b32 s0, s0, 7
	v_writelane_b32 v254, s0, 10
	s_lshl_b32 s0, s92, 3
	v_readlane_b32 s3, v254, 60
	s_add_i32 s2, s3, s0
	s_lshl_b32 s22, s83, 3
	s_cmp_lt_i32 s2, 0x8000
	v_writelane_b32 v255, s0, 4
	s_cselect_b64 s[0:1], -1, 0
	v_writelane_b32 v254, s0, 26
	v_and_b32_e32 v218, 15, v4
	v_bfe_u32 v219, v4, 4, 2
	v_writelane_b32 v254, s1, 27
	s_ashr_i32 s0, s2, 31
	s_lshr_b32 s0, s0, 22
	v_lshlrev_b32_e32 v4, 2, v4
	s_add_i32 s1, s2, s0
	v_lshlrev_b32_e32 v5, 4, v219
	v_lshlrev_b32_e32 v6, 6, v218
	v_and_b32_e32 v4, 32, v4
	s_ashr_i32 s0, s1, 10
	s_and_b32 s1, s1, 0xfffffc00
	v_bitop3_b32 v4, v6, v4, v5 bitop3:0x36
	s_sub_i32 s1, s2, s1
	v_add_u32_e32 v0, s4, v4
	s_ashr_i32 s4, s1, 31
	s_lshr_b32 s4, s4, 26
	s_add_i32 s8, s1, s4
	s_and_b32 s4, s8, 0x7ffffc0
	s_sub_i32 s12, s1, s4
	s_ashr_i32 s1, s0, 31
	v_readlane_b32 s84, v254, 2
	s_lshl_b64 s[4:5], s[0:1], 22
	s_lshl_b64 s[0:1], s[0:1], 24
	v_readlane_b32 s86, v254, 4
	v_readlane_b32 s88, v254, 6
	v_readlane_b32 s87, v254, 5
	s_mov_b32 s88, s13
	s_add_u32 s13, s86, s0
	s_addc_u32 s23, s87, s1
	s_lshl_b32 s0, s8, 1
	s_and_b32 s0, s0, 0xffffff80
	s_ashr_i32 s1, s0, 31
	v_readlane_b32 s90, v254, 8
	v_readlane_b32 s91, v254, 9
	s_mov_b32 s87, s9
	s_lshl_b64 s[8:9], s[0:1], 13
	s_mov_b64 s[90:91], s[24:25]
	s_add_u32 s24, s13, s8
	s_addc_u32 s23, s23, s9
	s_lshl_b32 s8, s12, 5
	s_ashr_i32 s9, s8, 31
	s_lshl_b64 s[12:13], s[8:9], 2
	s_add_u32 s12, s24, s12
	s_addc_u32 s13, s23, s13
	v_writelane_b32 v255, s12, 5
	s_waitcnt vmcnt(6)
	v_add_u32_e32 v1, 0, v4
	v_readlane_b32 s85, v254, 3
	v_writelane_b32 v255, s13, 6
	s_add_u32 s12, s63, s4
	s_addc_u32 s13, s64, s5
	s_lshl_b64 s[4:5], s[8:9], 11
	s_add_u32 s4, s12, s4
	s_addc_u32 s5, s13, s5
	s_add_u32 s0, s4, s0
	s_addc_u32 s1, s5, s1
	v_writelane_b32 v255, s0, 7
	v_readlane_b32 s89, v254, 7
	s_mov_b32 s69, 0x18000
	v_writelane_b32 v255, s1, 8
	s_add_i32 s0, s22, s2
	s_cmp_lt_i32 s0, 0x8000
	s_cselect_b64 s[0:1], -1, 0
	v_writelane_b32 v255, s0, 9
	s_lshl_b32 s29, s83, 4
	s_mov_b32 s71, 0x1a000
	s_mov_b32 s73, 0x8000
	s_mov_b32 s75, 0xa000
	s_mov_b32 s94, 0x1c000
	s_mov_b32 s96, 0x1e000
	v_add_u32_e32 v201, 0x10000, v0
	v_add_u32_e32 v220, 0x10400, v0
	v_add_u32_e32 v221, 0x10800, v0
	v_add_u32_e32 v222, 0x10c00, v0
	v_add_u32_e32 v223, 0x14000, v0
	v_add_u32_e32 v224, 0x14400, v0
	v_add_u32_e32 v225, 0x14800, v0
	v_add_u32_e32 v226, 0x14c00, v0
	v_add_u32_e32 v227, 0x18000, v0
	v_add_u32_e32 v228, 0x18400, v0
	v_add_u32_e32 v229, 0x18800, v0
	v_add_u32_e32 v230, 0x18c00, v0
	v_add_u32_e32 v231, 0x1c000, v0
	v_add_u32_e32 v232, 0x1c400, v0
	v_add_u32_e32 v233, 0x1c800, v0
	v_add_u32_e32 v234, 0x1cc00, v0
	s_mov_b32 s89, s20
	v_writelane_b32 v255, s1, 10
	s_add_i32 s28, s3, s29
	s_add_i32 s12, s3, s22
	s_mov_b32 s13, 0xc000
	s_mov_b32 s22, 0xe000
	s_mov_b32 s23, 0xc0e00000
	s_mov_b32 s24, 0xc3e00000
	s_mov_b32 s30, 0x43800000
	s_movk_i32 s25, 0x1000
	v_add_u32_e32 v235, s26, v1
	v_mov_b32_e32 v236, 0x40e00000
	v_mov_b32_e32 v237, 0x43e00000
	v_mov_b32_e32 v240, v64
	s_mov_b32 s26, 0
	v_readlane_b32 s85, v254, 58
	v_readlane_b32 s86, v254, 61
	s_barrier
	s_branch .LBB0_1520
